# baseline (speedup 1.0000x reference)
.LBB0_34:
	s_lshr_b32 s0, s2, 2
	s_and_b32 s0, s0, 0x3ffffffe
	s_and_b32 s1, s2, 1
	v_lshrrev_b32_e32 v143, 7, v0
	s_bfe_u32 s3, s2, 0x20001
	s_or_b32 s0, s0, s1
	v_lshl_or_b32 v133, s0, 1, v143
	s_mul_i32 s0, s3, 0xc0
	v_bfe_u32 v135, v0, 6, 1
	s_movk_i32 s1, 0x60
	v_mov_b32_e32 v2, s0
	v_lshrrev_b32_e32 v3, 2, v0
	v_mad_u32_u24 v2, v135, s1, v2
	v_and_b32_e32 v142, 8, v3
	v_or_b32_e32 v2, v2, v142
	v_lshl_add_u32 v130, v2, 7, v133
	v_mov_b32_e32 v131, 0
	v_lshlrev_b64 v[2:3], 9, v[130:131]
	v_mul_u32_u24_e32 v4, 0x60, v135
	s_waitcnt lgkmcnt(0)
	v_lshl_add_u64 v[2:3], s[4:5], 0, v[2:3]
	v_lshlrev_b32_e32 v130, 4, v1
	v_lshl_add_u64 v[136:137], v[2:3], 0, v[130:131]
	v_lshlrev_b32_e32 v130, 2, v4
	v_lshl_add_u64 v[2:3], s[6:7], 0, v[130:131]
	s_movk_i32 s2, 0x300
	v_mad_u64_u32 v[4:5], s[0:1], v11, s2, v[2:3]
	v_mad_u64_u32 v[2:3], s[0:1], v10, s2, v[2:3]
	s_mov_b32 s0, 0x10000
	s_nop 0
	v_add_co_u32_e32 v14, vcc, s0, v136
	s_mov_b32 s0, 0x20000
	s_nop 0
	v_addc_co_u32_e32 v15, vcc, 0, v137, vcc
	v_add_co_u32_e32 v32, vcc, s0, v136
	v_lshlrev_b32_e32 v130, 2, v142
	s_nop 0
	v_addc_co_u32_e32 v33, vcc, 0, v137, vcc
	s_mov_b32 s0, 0x30000
	v_lshl_add_u64 v[140:141], v[2:3], 0, v[130:131]
	v_add_co_u32_e32 v2, vcc, s0, v136
	s_mov_b32 s0, 0x40000
	s_nop 0
	v_addc_co_u32_e32 v3, vcc, 0, v137, vcc
	v_lshl_add_u64 v[138:139], v[4:5], 0, v[130:131]
	v_add_co_u32_e32 v4, vcc, s0, v136
	s_mov_b32 s0, 0x50000
	s_nop 0
	v_addc_co_u32_e32 v5, vcc, 0, v137, vcc
	v_add_co_u32_e32 v34, vcc, s0, v136
	global_load_dwordx4 v[16:19], v[2:3], off
	global_load_dwordx4 v[20:23], v[4:5], off
	s_nop 0
	global_load_dwordx4 v[2:5], v[140:141], off offset:16
	global_load_dwordx4 v[6:9], v[140:141], off
	global_load_dwordx4 v[10:13], v[138:139], off offset:16
	global_load_dwordx4 v[24:27], v[138:139], off
	v_addc_co_u32_e32 v35, vcc, 0, v137, vcc
	s_mov_b32 s0, 0x60000
	v_add_co_u32_e32 v36, vcc, s0, v136
	s_mov_b32 s0, 0x70000
	s_nop 0
	v_addc_co_u32_e32 v37, vcc, 0, v137, vcc
	global_load_dwordx4 v[28:31], v[34:35], off
	global_load_dwordx4 v[48:51], v[36:37], off
	v_add_co_u32_e32 v34, vcc, s0, v136
	s_mov_b32 s0, 0x100000
	s_nop 0
	v_addc_co_u32_e32 v35, vcc, 0, v137, vcc
	global_load_dwordx4 v[52:55], v[34:35], off
	global_load_dwordx4 v[56:59], v[14:15], off
	global_load_dwordx4 v[60:63], v[32:33], off
	global_load_dwordx4 v[144:147], v[136:137], off
	s_mov_b32 s2, 0xffff
	s_lshl_b32 s3, s3, 16
	s_or_b32 s4, s3, 0x4000
	s_or_b32 s5, s3, 0x8000
	s_or_b32 s6, s3, 0xc000
	s_waitcnt vmcnt(9)
	v_pk_mul_f32 v[2:3], v[2:3], v[132:133] op_sel_hi:[1,0]
	s_waitcnt vmcnt(8)
	v_pk_mul_f32 v[6:7], v[6:7], v[132:133] op_sel_hi:[1,0]
	v_pk_mul_f32 v[8:9], v[8:9], v[132:133] op_sel_hi:[1,0]
	v_pk_mul_f32 v[4:5], v[4:5], v[132:133] op_sel_hi:[1,0]
	s_waitcnt vmcnt(6)
	v_pk_mul_f32 v[14:15], v[24:25], v[134:135] op_sel_hi:[1,0]
	v_pk_mul_f32 v[32:33], v[26:27], v[134:135] op_sel_hi:[1,0]
	v_pk_mul_f32 v[10:11], v[10:11], v[134:135] op_sel_hi:[1,0]
	v_cvt_pk_f16_f32 v24, v6, v7
	v_pk_mul_f32 v[6:7], v[12:13], v[134:135] op_sel_hi:[1,0]
	v_cvt_pk_f16_f32 v25, v8, v9
	v_cvt_pk_f16_f32 v26, v2, v3
	v_cvt_pk_f16_f32 v27, v4, v5
	v_cvt_pk_f16_f32 v148, v14, v15
	v_cvt_pk_f16_f32 v149, v32, v33
	v_cvt_pk_f16_f32 v150, v10, v11
	v_cvt_pk_f16_f32 v151, v6, v7
	v_add_co_u32_e32 v2, vcc, s0, v136
	s_mov_b32 s0, 0x110000
	s_nop 0
	v_addc_co_u32_e32 v3, vcc, 0, v137, vcc
	global_load_dwordx4 v[152:155], v[2:3], off
	s_waitcnt vmcnt(4)
	v_cvt_pk_f16_f32 v5, v48, v52
	v_cvt_pk_f16_f32 v4, v20, v28
	s_waitcnt vmcnt(2)
	v_cvt_pk_f16_f32 v3, v60, v16
	s_waitcnt vmcnt(1)
	v_cvt_pk_f16_f32 v2, v144, v56
	v_cvt_pk_f16_f32 v84, v22, v30
	v_add_co_u32_e32 v22, vcc, s0, v136
	v_mfma_f32_32x32x16_f16 v[98:113], v[24:27], v[2:5], 0
	v_cvt_pk_f16_f32 v85, v50, v54
	v_cvt_pk_f16_f32 v83, v62, v18
	v_cvt_pk_f16_f32 v82, v146, v58
	v_cvt_pk_f16_f32 v20, v23, v31
	v_cvt_pk_f16_f32 v19, v63, v19
	v_cvt_pk_f16_f32 v18, v147, v59
	v_addc_co_u32_e32 v23, vcc, 0, v137, vcc
	v_mfma_f32_32x32x16_f16 v[66:81], v[148:151], v[2:5], 0
	v_cvt_pk_f16_f32 v5, v49, v53
	v_cvt_pk_f16_f32 v4, v21, v29
	v_cvt_pk_f16_f32 v3, v61, v17
	v_cvt_pk_f16_f32 v2, v145, v57
	v_cvt_pk_f16_f32 v21, v51, v55
	s_mov_b32 s0, 0x120000
	global_load_dwordx4 v[144:147], v[140:141], off offset:80
	global_load_dwordx4 v[156:159], v[140:141], off offset:64
	v_mfma_f32_32x32x16_f16 v[34:49], v[24:27], v[2:5], 0
	global_load_dwordx4 v[160:163], v[138:139], off offset:80
	global_load_dwordx4 v[164:167], v[138:139], off offset:64
	s_waitcnt vmcnt(3)
	v_mul_f32_e64 v144, v144, v132
	v_mul_f32_e64 v145, v145, v132
	v_mfma_f32_32x32x16_f16 v[114:129], v[24:27], v[82:85], 0
	v_mfma_f32_32x32x16_f16 v[50:65], v[24:27], v[18:21], 0
	v_add_co_u32_e32 v24, vcc, s0, v136
	s_mov_b32 s0, 0x130000
	s_nop 0
	v_addc_co_u32_e32 v25, vcc, 0, v137, vcc
	v_add_co_u32_e32 v26, vcc, s0, v136
	s_mov_b32 s0, 0x140000
	s_nop 0
	v_addc_co_u32_e32 v27, vcc, 0, v137, vcc
	v_add_co_u32_e32 v28, vcc, s0, v136
	s_mov_b32 s0, 0x150000
	s_nop 0
	v_addc_co_u32_e32 v29, vcc, 0, v137, vcc
	v_add_co_u32_e32 v30, vcc, s0, v136
	s_mov_b32 s0, 0x160000
	s_nop 0
	v_addc_co_u32_e32 v31, vcc, 0, v137, vcc
	v_add_co_u32_e32 v32, vcc, s0, v136
	s_mov_b32 s0, 0x170000
	s_nop 0
	v_addc_co_u32_e32 v33, vcc, 0, v137, vcc
	global_load_dwordx4 v[168:171], v[30:31], off
	global_load_dwordx4 v[172:175], v[32:33], off
	v_add_co_u32_e32 v30, vcc, s0, v136
	v_mfma_f32_32x32x16_f16 v[2:17], v[148:151], v[2:5], 0
	s_nop 0
	v_addc_co_u32_e32 v31, vcc, 0, v137, vcc
	global_load_dwordx4 v[176:179], v[30:31], off
	global_load_dwordx4 v[180:183], v[26:27], off
	global_load_dwordx4 v[184:187], v[28:29], off
	global_load_dwordx4 v[188:191], v[24:25], off
	global_load_dwordx4 v[192:195], v[22:23], off
	s_mov_b32 s0, 0x200000
	v_mfma_f32_32x32x16_f16 v[82:97], v[148:151], v[82:85], 0
	v_mfma_f32_32x32x16_f16 v[18:33], v[148:151], v[18:21], 0
	s_waitcnt vmcnt(9)
	v_mul_f32_e64 v148, v156, v132
	v_mul_f32_e64 v149, v157, v132
	v_mul_f32_e64 v150, v158, v132
	v_mul_f32_e64 v151, v159, v132
	v_cvt_pk_f16_f32 v148, v148, v149
	v_cvt_pk_f16_f32 v149, v150, v151
	v_cvt_pk_f16_f32 v150, v144, v145
	v_pk_mul_f32 v[144:145], v[146:147], v[132:133] op_sel_hi:[1,0]
	s_waitcnt vmcnt(7)
	v_pk_mul_f32 v[146:147], v[166:167], v[134:135] op_sel_hi:[1,0]
	v_cvt_pk_f16_f32 v151, v144, v145
	v_pk_mul_f32 v[144:145], v[164:165], v[134:135] op_sel_hi:[1,0]
	v_add_co_u32_e32 v156, vcc, s0, v136
	v_cvt_pk_f16_f32 v144, v144, v145
	v_cvt_pk_f16_f32 v145, v146, v147
	v_pk_mul_f32 v[146:147], v[160:161], v[134:135] op_sel_hi:[1,0]
	v_pk_mul_f32 v[160:161], v[162:163], v[134:135] op_sel_hi:[1,0]
	v_addc_co_u32_e32 v157, vcc, 0, v137, vcc
	v_cvt_pk_f16_f32 v146, v146, v147
	v_cvt_pk_f16_f32 v147, v160, v161
	s_mov_b32 s0, 0x210000
	v_add_co_u32_e32 v196, vcc, s0, v136
	s_mov_b32 s0, 0x220000
	s_nop 0
	v_addc_co_u32_e32 v197, vcc, 0, v137, vcc
	global_load_dwordx4 v[156:159], v[156:157], off
	s_waitcnt vmcnt(5)
	v_cvt_pk_f16_f32 v163, v173, v177
	v_cvt_pk_f16_f32 v167, v172, v176
	s_waitcnt vmcnt(3)
	v_cvt_pk_f16_f32 v162, v185, v169
	s_waitcnt vmcnt(2)
	v_cvt_pk_f16_f32 v161, v189, v181
	s_waitcnt vmcnt(1)
	v_cvt_pk_f16_f32 v164, v152, v192
	v_add_co_u32_e32 v192, vcc, s0, v136
	v_cvt_pk_f16_f32 v160, v153, v193
	s_nop 0
	v_addc_co_u32_e32 v193, vcc, 0, v137, vcc
	s_mov_b32 s0, 0x230000
	v_cvt_pk_f16_f32 v166, v184, v168
	v_mfma_f32_32x32x16_f16 v[34:49], v[148:151], v[160:163], v[34:49]
	v_add_co_u32_e32 v184, vcc, s0, v136
	v_cvt_pk_f16_f32 v165, v188, v180
	s_nop 0
	v_addc_co_u32_e32 v185, vcc, 0, v137, vcc
	s_mov_b32 s0, 0x240000
	v_add_co_u32_e32 v188, vcc, s0, v136
	v_mfma_f32_32x32x16_f16 v[2:17], v[144:147], v[160:163], v[2:17]
	v_cvt_pk_f16_f32 v163, v174, v178
	v_cvt_pk_f16_f32 v162, v186, v170
	v_cvt_pk_f16_f32 v161, v190, v182
	v_cvt_pk_f16_f32 v160, v154, v194
	v_addc_co_u32_e32 v189, vcc, 0, v137, vcc
	s_mov_b32 s0, 0x250000
	v_mfma_f32_32x32x16_f16 v[114:129], v[148:151], v[160:163], v[114:129]
	v_add_co_u32_e32 v172, vcc, s0, v136
	s_mov_b32 s0, 0x260000
	s_nop 0
	v_addc_co_u32_e32 v173, vcc, 0, v137, vcc
	v_add_co_u32_e32 v176, vcc, s0, v136
	v_mfma_f32_32x32x16_f16 v[82:97], v[144:147], v[160:163], v[82:97]
	v_cvt_pk_f16_f32 v163, v175, v179
	v_cvt_pk_f16_f32 v162, v187, v171
	v_cvt_pk_f16_f32 v161, v191, v183
	v_cvt_pk_f16_f32 v160, v155, v195
	v_addc_co_u32_e32 v177, vcc, 0, v137, vcc
	s_mov_b32 s0, 0x270000
	v_mfma_f32_32x32x16_f16 v[98:113], v[148:151], v[164:167], v[98:113]
	v_add_co_u32_e32 v180, vcc, s0, v136
	s_mov_b32 s0, 0x300000
	s_nop 0
	v_addc_co_u32_e32 v181, vcc, 0, v137, vcc
	v_mfma_f32_32x32x16_f16 v[50:65], v[148:151], v[160:163], v[50:65]
	global_load_dwordx4 v[148:151], v[140:141], off offset:144
	global_load_dwordx4 v[152:155], v[140:141], off offset:128
	v_mfma_f32_32x32x16_f16 v[66:81], v[144:147], v[164:167], v[66:81]
	global_load_dwordx4 v[164:167], v[138:139], off offset:144
	global_load_dwordx4 v[168:171], v[138:139], off offset:128
	s_nop 0
	global_load_dwordx4 v[172:175], v[172:173], off
	s_nop 0
	global_load_dwordx4 v[176:179], v[176:177], off
	s_nop 0
	global_load_dwordx4 v[180:183], v[180:181], off
	s_nop 0
	global_load_dwordx4 v[184:187], v[184:185], off
	s_nop 0
	global_load_dwordx4 v[188:191], v[188:189], off
	s_nop 0
	global_load_dwordx4 v[192:195], v[192:193], off
	s_nop 0
	global_load_dwordx4 v[196:199], v[196:197], off
	v_mfma_f32_32x32x16_f16 v[18:33], v[144:147], v[160:163], v[18:33]
	s_waitcnt vmcnt(9)
	v_mul_f32_e64 v144, v152, v132
	v_mul_f32_e64 v145, v153, v132
	v_mul_f32_e64 v146, v154, v132
	v_mul_f32_e64 v147, v155, v132
	v_cvt_pk_f16_f32 v144, v144, v145
	v_cvt_pk_f16_f32 v145, v146, v147
	v_pk_mul_f32 v[146:147], v[148:149], v[132:133] op_sel_hi:[1,0]
	v_pk_mul_f32 v[148:149], v[150:151], v[132:133] op_sel_hi:[1,0]
	v_cvt_pk_f16_f32 v146, v146, v147
	v_cvt_pk_f16_f32 v147, v148, v149
	s_waitcnt vmcnt(7)
	v_pk_mul_f32 v[148:149], v[168:169], v[134:135] op_sel_hi:[1,0]
	v_pk_mul_f32 v[150:151], v[170:171], v[134:135] op_sel_hi:[1,0]
	v_cvt_pk_f16_f32 v148, v148, v149
	v_cvt_pk_f16_f32 v149, v150, v151
	v_pk_mul_f32 v[150:151], v[164:165], v[134:135] op_sel_hi:[1,0]
	v_pk_mul_f32 v[164:165], v[166:167], v[134:135] op_sel_hi:[1,0]
	v_cvt_pk_f16_f32 v150, v150, v151
	v_cvt_pk_f16_f32 v151, v164, v165
	v_add_co_u32_e32 v152, vcc, s0, v136
	s_mov_b32 s0, 0x310000
	s_nop 0
	v_addc_co_u32_e32 v153, vcc, 0, v137, vcc
	s_waitcnt vmcnt(4)
	v_cvt_pk_f16_f32 v163, v176, v180
	s_waitcnt vmcnt(2)
	v_cvt_pk_f16_f32 v162, v188, v172
	s_waitcnt vmcnt(1)
	v_cvt_pk_f16_f32 v161, v192, v184
	s_waitcnt vmcnt(0)
	v_cvt_pk_f16_f32 v160, v156, v196
	v_add_co_u32_e32 v196, vcc, s0, v136
	s_nop 0
	v_mfma_f32_32x32x16_f16 v[98:113], v[144:147], v[160:163], v[98:113]
	s_mov_b32 s0, 0x320000
	global_load_dwordx4 v[152:155], v[152:153], off
	v_mfma_f32_32x32x16_f16 v[66:81], v[148:151], v[160:163], v[66:81]
	v_cvt_pk_f16_f32 v160, v157, v197
	v_addc_co_u32_e32 v197, vcc, 0, v137, vcc
	v_add_co_u32_e32 v192, vcc, s0, v136
	v_cvt_pk_f16_f32 v163, v177, v181
	v_cvt_pk_f16_f32 v162, v189, v173
	v_cvt_pk_f16_f32 v161, v193, v185
	v_addc_co_u32_e32 v193, vcc, 0, v137, vcc
	s_mov_b32 s0, 0x330000
	v_mfma_f32_32x32x16_f16 v[34:49], v[144:147], v[160:163], v[34:49]
	v_add_co_u32_e32 v184, vcc, s0, v136
	s_mov_b32 s0, 0x340000
	s_nop 0
	v_addc_co_u32_e32 v185, vcc, 0, v137, vcc
	v_add_co_u32_e32 v188, vcc, s0, v136
	v_mfma_f32_32x32x16_f16 v[2:17], v[148:151], v[160:163], v[2:17]
	v_cvt_pk_f16_f32 v163, v178, v182
	v_cvt_pk_f16_f32 v162, v190, v174
	v_cvt_pk_f16_f32 v161, v194, v186
	v_cvt_pk_f16_f32 v160, v158, v198
	v_addc_co_u32_e32 v189, vcc, 0, v137, vcc
	s_mov_b32 s0, 0x350000
	v_mfma_f32_32x32x16_f16 v[114:129], v[144:147], v[160:163], v[114:129]
	v_add_co_u32_e32 v172, vcc, s0, v136
	s_mov_b32 s0, 0x360000
	s_nop 0
	v_addc_co_u32_e32 v173, vcc, 0, v137, vcc
	v_add_co_u32_e32 v176, vcc, s0, v136
	v_mfma_f32_32x32x16_f16 v[82:97], v[148:151], v[160:163], v[82:97]
	v_cvt_pk_f16_f32 v163, v179, v183
	v_cvt_pk_f16_f32 v162, v191, v175
	v_cvt_pk_f16_f32 v161, v195, v187
	v_cvt_pk_f16_f32 v160, v159, v199
	v_addc_co_u32_e32 v177, vcc, 0, v137, vcc
	s_mov_b32 s0, 0x370000
	v_mfma_f32_32x32x16_f16 v[50:65], v[144:147], v[160:163], v[50:65]
	global_load_dwordx4 v[144:147], v[140:141], off offset:208
	global_load_dwordx4 v[156:159], v[140:141], off offset:192
	global_load_dwordx4 v[164:167], v[138:139], off offset:208
	global_load_dwordx4 v[168:171], v[138:139], off offset:192
	v_add_co_u32_e32 v180, vcc, s0, v136
	global_load_dwordx4 v[172:175], v[172:173], off
	s_nop 0
	global_load_dwordx4 v[176:179], v[176:177], off
	v_addc_co_u32_e32 v181, vcc, 0, v137, vcc
	global_load_dwordx4 v[180:183], v[180:181], off
	s_nop 0
	global_load_dwordx4 v[184:187], v[184:185], off
	s_nop 0
	global_load_dwordx4 v[188:191], v[188:189], off
	s_nop 0
	global_load_dwordx4 v[192:195], v[192:193], off
	s_nop 0
	global_load_dwordx4 v[196:199], v[196:197], off
	v_mfma_f32_32x32x16_f16 v[18:33], v[148:151], v[160:163], v[18:33]
	s_mov_b32 s0, 0x400000
	s_waitcnt vmcnt(10)
	v_mul_f32_e64 v144, v144, v132
	v_mul_f32_e64 v145, v145, v132
	s_waitcnt vmcnt(9)
	v_pk_mul_f32 v[148:149], v[156:157], v[132:133] op_sel_hi:[1,0]
	v_pk_mul_f32 v[150:151], v[158:159], v[132:133] op_sel_hi:[1,0]
	v_cvt_pk_f16_f32 v148, v148, v149
	v_cvt_pk_f16_f32 v149, v150, v151
	v_cvt_pk_f16_f32 v150, v144, v145
	v_pk_mul_f32 v[144:145], v[146:147], v[132:133] op_sel_hi:[1,0]
	s_waitcnt vmcnt(7)
	v_pk_mul_f32 v[146:147], v[170:171], v[134:135] op_sel_hi:[1,0]
	v_cvt_pk_f16_f32 v151, v144, v145
	v_pk_mul_f32 v[144:145], v[168:169], v[134:135] op_sel_hi:[1,0]
	v_add_co_u32_e32 v156, vcc, s0, v136
	v_cvt_pk_f16_f32 v144, v144, v145
	v_cvt_pk_f16_f32 v145, v146, v147
	v_pk_mul_f32 v[146:147], v[164:165], v[134:135] op_sel_hi:[1,0]
	v_pk_mul_f32 v[164:165], v[166:167], v[134:135] op_sel_hi:[1,0]
	v_cvt_pk_f16_f32 v146, v146, v147
	v_cvt_pk_f16_f32 v147, v164, v165
	v_addc_co_u32_e32 v157, vcc, 0, v137, vcc
	s_mov_b32 s0, 0x410000
	s_waitcnt vmcnt(4)
	v_cvt_pk_f16_f32 v163, v176, v180
	s_waitcnt vmcnt(2)
	v_cvt_pk_f16_f32 v162, v188, v172
	s_waitcnt vmcnt(1)
	v_cvt_pk_f16_f32 v161, v192, v184
	s_waitcnt vmcnt(0)
	v_cvt_pk_f16_f32 v160, v152, v196
	v_add_co_u32_e32 v196, vcc, s0, v136
	s_nop 0
	v_mfma_f32_32x32x16_f16 v[98:113], v[148:151], v[160:163], v[98:113]
	s_mov_b32 s0, 0x420000
	global_load_dwordx4 v[156:159], v[156:157], off
	v_mfma_f32_32x32x16_f16 v[66:81], v[144:147], v[160:163], v[66:81]
	v_cvt_pk_f16_f32 v160, v153, v197
	v_addc_co_u32_e32 v197, vcc, 0, v137, vcc
	v_add_co_u32_e32 v192, vcc, s0, v136
	v_cvt_pk_f16_f32 v163, v177, v181
	v_cvt_pk_f16_f32 v162, v189, v173
	v_cvt_pk_f16_f32 v161, v193, v185
	v_addc_co_u32_e32 v193, vcc, 0, v137, vcc
	s_mov_b32 s0, 0x430000
	v_mfma_f32_32x32x16_f16 v[34:49], v[148:151], v[160:163], v[34:49]
	v_add_co_u32_e32 v184, vcc, s0, v136
	s_mov_b32 s0, 0x440000
	s_nop 0
	v_addc_co_u32_e32 v185, vcc, 0, v137, vcc
	v_add_co_u32_e32 v188, vcc, s0, v136
	v_mfma_f32_32x32x16_f16 v[2:17], v[144:147], v[160:163], v[2:17]
	v_cvt_pk_f16_f32 v163, v178, v182
	v_cvt_pk_f16_f32 v162, v190, v174
	v_cvt_pk_f16_f32 v161, v194, v186
	v_cvt_pk_f16_f32 v160, v154, v198
	v_addc_co_u32_e32 v189, vcc, 0, v137, vcc
	s_mov_b32 s0, 0x450000
	v_mfma_f32_32x32x16_f16 v[114:129], v[148:151], v[160:163], v[114:129]
	v_add_co_u32_e32 v172, vcc, s0, v136
	s_mov_b32 s0, 0x460000
	s_nop 0
	v_addc_co_u32_e32 v173, vcc, 0, v137, vcc
	v_add_co_u32_e32 v176, vcc, s0, v136
	v_mfma_f32_32x32x16_f16 v[82:97], v[144:147], v[160:163], v[82:97]
	v_cvt_pk_f16_f32 v163, v179, v183
	v_cvt_pk_f16_f32 v162, v191, v175
	v_cvt_pk_f16_f32 v161, v195, v187
	v_cvt_pk_f16_f32 v160, v155, v199
	v_addc_co_u32_e32 v177, vcc, 0, v137, vcc
	s_mov_b32 s0, 0x470000
	v_mfma_f32_32x32x16_f16 v[50:65], v[148:151], v[160:163], v[50:65]
	global_load_dwordx4 v[148:151], v[140:141], off offset:272
	global_load_dwordx4 v[152:155], v[140:141], off offset:256
	global_load_dwordx4 v[164:167], v[138:139], off offset:272
	global_load_dwordx4 v[168:171], v[138:139], off offset:256
	v_add_co_u32_e32 v180, vcc, s0, v136
	global_load_dwordx4 v[172:175], v[172:173], off
	s_nop 0
	global_load_dwordx4 v[176:179], v[176:177], off
	v_addc_co_u32_e32 v181, vcc, 0, v137, vcc
	global_load_dwordx4 v[180:183], v[180:181], off
	s_nop 0
	global_load_dwordx4 v[184:187], v[184:185], off
	s_nop 0
	global_load_dwordx4 v[188:191], v[188:189], off
	s_nop 0
	global_load_dwordx4 v[192:195], v[192:193], off
	s_nop 0
	global_load_dwordx4 v[196:199], v[196:197], off
	v_mfma_f32_32x32x16_f16 v[18:33], v[144:147], v[160:163], v[18:33]
	s_mov_b32 s0, 0x500000
	s_waitcnt vmcnt(9)
	v_mul_f32_e64 v144, v152, v132
	v_mul_f32_e64 v145, v153, v132
	v_mul_f32_e64 v146, v154, v132
	v_mul_f32_e64 v147, v155, v132
	v_cvt_pk_f16_f32 v144, v144, v145
	v_cvt_pk_f16_f32 v145, v146, v147
	v_pk_mul_f32 v[146:147], v[148:149], v[132:133] op_sel_hi:[1,0]
	v_pk_mul_f32 v[148:149], v[150:151], v[132:133] op_sel_hi:[1,0]
	v_cvt_pk_f16_f32 v146, v146, v147
	v_cvt_pk_f16_f32 v147, v148, v149
	s_waitcnt vmcnt(7)
	v_pk_mul_f32 v[148:149], v[168:169], v[134:135] op_sel_hi:[1,0]
	v_pk_mul_f32 v[150:151], v[170:171], v[134:135] op_sel_hi:[1,0]
	v_cvt_pk_f16_f32 v148, v148, v149
	v_cvt_pk_f16_f32 v149, v150, v151
	v_pk_mul_f32 v[150:151], v[164:165], v[134:135] op_sel_hi:[1,0]
	v_pk_mul_f32 v[164:165], v[166:167], v[134:135] op_sel_hi:[1,0]
	v_cvt_pk_f16_f32 v150, v150, v151
	v_cvt_pk_f16_f32 v151, v164, v165
	v_add_co_u32_e32 v152, vcc, s0, v136
	s_mov_b32 s0, 0x510000
	s_nop 0
	v_addc_co_u32_e32 v153, vcc, 0, v137, vcc
	s_waitcnt vmcnt(4)
	v_cvt_pk_f16_f32 v163, v176, v180
	s_waitcnt vmcnt(2)
	v_cvt_pk_f16_f32 v162, v188, v172
	s_waitcnt vmcnt(1)
	v_cvt_pk_f16_f32 v161, v192, v184
	s_waitcnt vmcnt(0)
	v_cvt_pk_f16_f32 v160, v156, v196
	v_add_co_u32_e32 v192, vcc, s0, v136
	s_nop 0
	v_mfma_f32_32x32x16_f16 v[98:113], v[144:147], v[160:163], v[98:113]
	s_mov_b32 s0, 0x520000
	global_load_dwordx4 v[152:155], v[152:153], off
	v_mfma_f32_32x32x16_f16 v[66:81], v[148:151], v[160:163], v[66:81]
	v_cvt_pk_f16_f32 v161, v193, v185
	v_addc_co_u32_e32 v193, vcc, 0, v137, vcc
	v_add_co_u32_e32 v188, vcc, s0, v136
	v_cvt_pk_f16_f32 v162, v189, v173
	s_nop 0
	v_addc_co_u32_e32 v189, vcc, 0, v137, vcc
	s_mov_b32 s0, 0x530000
	v_add_co_u32_e32 v180, vcc, s0, v136
	v_cvt_pk_f16_f32 v163, v177, v181
	v_cvt_pk_f16_f32 v160, v157, v197
	v_addc_co_u32_e32 v181, vcc, 0, v137, vcc
	s_mov_b32 s0, 0x540000
	v_mfma_f32_32x32x16_f16 v[34:49], v[144:147], v[160:163], v[34:49]
	v_add_co_u32_e32 v184, vcc, s0, v136
	s_mov_b32 s0, 0x550000
	s_nop 0
	v_addc_co_u32_e32 v185, vcc, 0, v137, vcc
	v_add_co_u32_e32 v164, vcc, s0, v136
	v_mfma_f32_32x32x16_f16 v[2:17], v[148:151], v[160:163], v[2:17]
	v_cvt_pk_f16_f32 v163, v178, v182
	v_cvt_pk_f16_f32 v162, v190, v174
	v_cvt_pk_f16_f32 v161, v194, v186
	v_cvt_pk_f16_f32 v160, v158, v198
	v_addc_co_u32_e32 v165, vcc, 0, v137, vcc
	s_mov_b32 s0, 0x560000
	v_mfma_f32_32x32x16_f16 v[114:129], v[144:147], v[160:163], v[114:129]
	v_mfma_f32_32x32x16_f16 v[82:97], v[148:151], v[160:163], v[82:97]
	v_cvt_pk_f16_f32 v163, v179, v183
	v_cvt_pk_f16_f32 v162, v191, v175
	v_cvt_pk_f16_f32 v161, v195, v187
	v_cvt_pk_f16_f32 v160, v159, v199
	s_nop 1
	v_mfma_f32_32x32x16_f16 v[50:65], v[144:147], v[160:163], v[50:65]
	global_load_dwordx4 v[144:147], v[140:141], off offset:336
	global_load_dwordx4 v[156:159], v[140:141], off offset:320
	v_add_co_u32_e32 v140, vcc, s0, v136
	s_mov_b32 s0, 0x570000
	s_nop 0
	v_addc_co_u32_e32 v141, vcc, 0, v137, vcc
	global_load_dwordx4 v[164:167], v[164:165], off
	s_nop 0
	global_load_dwordx4 v[168:171], v[140:141], off
	global_load_dwordx4 v[172:175], v[138:139], off offset:336
	s_nop 0
	global_load_dwordx4 v[138:141], v[138:139], off offset:320
	v_add_co_u32_e32 v136, vcc, s0, v136
	v_mfma_f32_32x32x16_f16 v[18:33], v[148:151], v[160:163], v[18:33]
	s_nop 0
	v_addc_co_u32_e32 v137, vcc, 0, v137, vcc
	global_load_dwordx4 v[176:179], v[136:137], off
	s_nop 0
	global_load_dwordx4 v[180:183], v[180:181], off
	s_nop 0
	global_load_dwordx4 v[184:187], v[184:185], off
	s_nop 0
	global_load_dwordx4 v[188:191], v[188:189], off
	s_nop 0
	global_load_dwordx4 v[192:195], v[192:193], off
	v_cmp_eq_u32_e32 vcc, 0, v135
	s_waitcnt vmcnt(9)
	v_pk_mul_f32 v[136:137], v[156:157], v[132:133] op_sel_hi:[1,0]
	s_nop 0
	v_cvt_pk_f16_f32 v148, v136, v137
	v_pk_mul_f32 v[136:137], v[158:159], v[132:133] op_sel_hi:[1,0]
	s_nop 0
	v_cvt_pk_f16_f32 v149, v136, v137
	v_pk_mul_f32 v[136:137], v[144:145], v[132:133] op_sel_hi:[1,0]
	s_waitcnt vmcnt(1)
	v_cvt_pk_f16_f32 v145, v188, v180
	v_cvt_pk_f16_f32 v150, v136, v137
	v_pk_mul_f32 v[136:137], v[146:147], v[132:133] op_sel_hi:[1,0]
	v_cvt_pk_f16_f32 v147, v168, v176
	v_cvt_pk_f16_f32 v151, v136, v137
	v_pk_mul_f32 v[136:137], v[138:139], v[134:135] op_sel_hi:[1,0]
	v_pk_mul_f32 v[138:139], v[140:141], v[134:135] op_sel_hi:[1,0]
	v_cvt_pk_f16_f32 v136, v136, v137
	v_cvt_pk_f16_f32 v137, v138, v139
	v_pk_mul_f32 v[138:139], v[172:173], v[134:135] op_sel_hi:[1,0]
	v_pk_mul_f32 v[140:141], v[174:175], v[134:135] op_sel_hi:[1,0]
	v_cvt_pk_f16_f32 v138, v138, v139
	v_cvt_pk_f16_f32 v139, v140, v141
	v_cvt_pk_f16_f32 v146, v184, v164
	s_waitcnt vmcnt(0)
	v_cvt_pk_f16_f32 v144, v152, v192
	v_and_b32_e32 v132, 63, v0
	v_lshlrev_b32_e32 v0, 2, v132
	v_mfma_f32_32x32x16_f16 v[98:113], v[148:151], v[144:147], v[98:113]
	v_lshl_or_b32 v140, v143, 15, v0
	v_lshlrev_b32_e32 v141, 14, v135
	v_or_b32_e32 v130, v140, v141
	v_mfma_f32_32x32x16_f16 v[66:81], v[136:139], v[144:147], v[66:81]
	v_cvt_pk_f16_f32 v147, v169, v177
	v_cvt_pk_f16_f32 v146, v185, v165
	v_cvt_pk_f16_f32 v145, v189, v181
	v_cvt_pk_f16_f32 v144, v153, v193
	s_nop 1
	v_mfma_f32_32x32x16_f16 v[34:49], v[148:151], v[144:147], v[34:49]
	v_mfma_f32_32x32x16_f16 v[2:17], v[136:139], v[144:147], v[2:17]
	v_cvt_pk_f16_f32 v147, v170, v178
	v_cvt_pk_f16_f32 v146, v186, v166
	v_cvt_pk_f16_f32 v145, v190, v182
	v_cvt_pk_f16_f32 v144, v154, v194
	s_nop 1
	v_mfma_f32_32x32x16_f16 v[114:129], v[148:151], v[144:147], v[114:129]
	v_mfma_f32_32x32x16_f16 v[82:97], v[136:139], v[144:147], v[82:97]
	s_nop 10
	s_cbranch_vccz .Lk1_role1
	ds_write2st64_b32 v130, v114, v115 offset1:1
	ds_write2st64_b32 v130, v116, v117 offset0:2 offset1:3
	ds_write2st64_b32 v130, v118, v119 offset0:4 offset1:5
	ds_write2st64_b32 v130, v120, v121 offset0:6 offset1:7
	ds_write2st64_b32 v130, v122, v123 offset0:8 offset1:9
	ds_write2st64_b32 v130, v124, v125 offset0:10 offset1:11
	v_cvt_pk_f16_f32 v147, v171, v179
	v_cvt_pk_f16_f32 v146, v187, v167
	v_cvt_pk_f16_f32 v145, v191, v183
	v_cvt_pk_f16_f32 v144, v155, v195
	ds_write2st64_b32 v130, v126, v127 offset0:12 offset1:13
	s_nop 1
	v_mfma_f32_32x32x16_f16 v[50:65], v[148:151], v[144:147], v[50:65]
	ds_write2st64_b32 v130, v128, v129 offset0:14 offset1:15
	ds_write2st64_b32 v130, v82, v83 offset0:16 offset1:17
	ds_write2st64_b32 v130, v84, v85 offset0:18 offset1:19
	ds_write2st64_b32 v130, v86, v87 offset0:20 offset1:21
	ds_write2st64_b32 v130, v88, v89 offset0:22 offset1:23
	ds_write2st64_b32 v130, v90, v91 offset0:24 offset1:25
	ds_write2st64_b32 v130, v92, v93 offset0:26 offset1:27
	ds_write2st64_b32 v130, v94, v95 offset0:28 offset1:29
	s_nop 1
	v_mfma_f32_32x32x16_f16 v[18:33], v[136:139], v[144:147], v[18:33]
	s_nop 11
	ds_write2st64_b32 v130, v96, v97 offset0:30 offset1:31
	ds_write2st64_b32 v130, v50, v51 offset0:32 offset1:33
	ds_write2st64_b32 v130, v52, v53 offset0:34 offset1:35
	ds_write2st64_b32 v130, v54, v55 offset0:36 offset1:37
	ds_write2st64_b32 v130, v56, v57 offset0:38 offset1:39
	ds_write2st64_b32 v130, v58, v59 offset0:40 offset1:41
	ds_write2st64_b32 v130, v60, v61 offset0:42 offset1:43
	ds_write2st64_b32 v130, v62, v63 offset0:44 offset1:45
	ds_write2st64_b32 v130, v64, v65 offset0:46 offset1:47
	ds_write2st64_b32 v130, v18, v19 offset0:48 offset1:49
	ds_write2st64_b32 v130, v20, v21 offset0:50 offset1:51
	ds_write2st64_b32 v130, v22, v23 offset0:52 offset1:53
	ds_write2st64_b32 v130, v24, v25 offset0:54 offset1:55
	ds_write2st64_b32 v130, v26, v27 offset0:56 offset1:57
	ds_write2st64_b32 v130, v28, v29 offset0:58 offset1:59
	ds_write2st64_b32 v130, v30, v31 offset0:60 offset1:61
	ds_write2st64_b32 v130, v32, v33 offset0:62 offset1:63
	v_lshlrev_b32_e32 v0, 2, v1
	v_lshl_or_b32 v143, v135, 1, v0
	v_mbcnt_lo_u32_b32 v0, -1, 0
	v_mbcnt_hi_u32_b32 v0, -1, v0
	v_and_b32_e32 v130, 64, v0
	v_xor_b32_e32 v1, 32, v0
	v_add_u32_e32 v130, 64, v130
	v_cmp_lt_i32_e64 s[0:1], v1, v130
	v_lshlrev_b32_e32 v130, 1, v142
	s_waitcnt lgkmcnt(0)
	v_cndmask_b32_e64 v0, v0, v1, s[0:1]
	v_lshlrev_b32_e32 v144, 2, v0
	v_xor_b32_e32 v0, 0x4000, v141
	v_or_b32_e32 v142, v140, v0
	s_barrier
	ds_read2st64_b32 v[0:1], v142 offset1:1
	ds_read2st64_b32 v[134:135], v142 offset0:4 offset1:5
	ds_read2st64_b32 v[136:137], v142 offset0:6 offset1:7
	ds_read2st64_b32 v[138:139], v142 offset0:2 offset1:3
	s_waitcnt lgkmcnt(3)
	v_add_f32_e32 v0, v98, v0
	s_waitcnt lgkmcnt(2)
	v_add_f32_e32 v98, v102, v134
	v_add_f32_e32 v1, v99, v1
	v_add_f32_e32 v99, v103, v135
	s_waitcnt lgkmcnt(0)
	v_add_f32_e32 v100, v100, v138
	v_add_f32_e32 v102, v104, v136
	v_add_f32_e32 v101, v101, v139
	v_cvt_pk_f16_f32 v104, v0, v1
	v_add_f32_e32 v0, v105, v137
	v_cvt_pk_f16_f32 v100, v100, v101
	v_cvt_pk_f16_f32 v101, v98, v99
	v_cvt_pk_f16_f32 v102, v102, v0
	v_cmp_gt_u32_e64 s[0:1], 32, v132
	v_mov_b32_e32 v120, 0x3c00
	v_bfrev_b32_e32 v121, 60
	v_cndmask_b32_e64 v0, v100, v102, s[0:1]
	v_cndmask_b32_e64 v1, v104, v101, s[0:1]
	ds_bpermute_b32 v103, v144, v0
	ds_bpermute_b32 v105, v144, v1
	v_lshlrev_b32_e32 v145, 7, v133
	s_waitcnt lgkmcnt(1)
	v_cndmask_b32_e64 v99, v103, v100, s[0:1]
	v_cndmask_b32_e64 v100, v102, v103, s[0:1]
	s_waitcnt lgkmcnt(0)
	v_cndmask_b32_e64 v102, v101, v105, s[0:1]
	v_cndmask_b32_e64 v103, v120, v102, s[0:1]
	v_cndmask_b32_e64 v101, v121, v100, s[0:1]
	v_cndmask_b32_e64 v98, v105, v104, s[0:1]
	v_bfi_b32 v101, s2, v100, v101
	v_bfi_b32 v100, s2, v103, v102
	ds_read2st64_b32 v[102:103], v142 offset0:8 offset1:9
	ds_read2st64_b32 v[104:105], v142 offset0:12 offset1:13
	ds_read2st64_b32 v[114:115], v142 offset0:14 offset1:15
	ds_read2st64_b32 v[116:117], v142 offset0:10 offset1:11
	v_or_b32_e32 v119, v143, v145
	v_lshl_add_u64 v[0:1], s[8:9], 0, v[130:131]
	s_waitcnt lgkmcnt(3)
	v_add_f32_e32 v102, v106, v102
	v_add_f32_e32 v103, v107, v103
	s_waitcnt lgkmcnt(2)
	v_add_f32_e32 v105, v111, v105
	v_add_f32_e32 v104, v110, v104
	s_waitcnt lgkmcnt(0)
	v_add_f32_e32 v106, v108, v116
	v_add_f32_e32 v107, v112, v114
	v_add_f32_e32 v108, v109, v117
	v_cvt_pk_f16_f32 v110, v102, v103
	v_add_f32_e32 v102, v113, v115
	v_cvt_pk_f16_f32 v106, v106, v108
	v_cvt_pk_f16_f32 v104, v104, v105
	v_cvt_pk_f16_f32 v105, v107, v102
	v_cndmask_b32_e64 v102, v106, v105, s[0:1]
	v_cndmask_b32_e64 v103, v110, v104, s[0:1]
	ds_bpermute_b32 v107, v144, v102
	ds_bpermute_b32 v108, v144, v103
	v_add_u32_e32 v130, s3, v119
	v_lshlrev_b64 v[102:103], 5, v[130:131]
	v_lshl_add_u64 v[102:103], v[0:1], 0, v[102:103]
	global_store_dwordx4 v[102:103], v[98:101], off
	s_waitcnt lgkmcnt(0)
	v_cndmask_b32_e64 v102, v104, v108, s[0:1]
	v_cndmask_b32_e64 v100, v105, v107, s[0:1]
	v_xor_b32_e32 v82, 0x5000, v141
	v_cndmask_b32_e64 v98, v108, v110, s[0:1]
	v_cndmask_b32_e64 v103, v120, v102, s[0:1]
	v_cndmask_b32_e64 v101, v121, v100, s[0:1]
	v_or_b32_e32 v110, v140, v82
	v_cndmask_b32_e64 v99, v107, v106, s[0:1]
	v_bfi_b32 v101, s2, v100, v101
	v_bfi_b32 v100, s2, v103, v102
	ds_read2st64_b32 v[102:103], v110 offset1:1
	ds_read2st64_b32 v[104:105], v110 offset0:4 offset1:5
	ds_read2st64_b32 v[106:107], v110 offset0:6 offset1:7
	ds_read2st64_b32 v[108:109], v110 offset0:2 offset1:3
	s_waitcnt lgkmcnt(3)
	v_add_f32_e32 v66, v66, v102
	v_add_f32_e32 v67, v67, v103
	s_waitcnt lgkmcnt(2)
	v_add_f32_e32 v70, v70, v104
	v_add_f32_e32 v71, v71, v105
	s_waitcnt lgkmcnt(0)
	v_add_f32_e32 v68, v68, v108
	v_add_f32_e32 v72, v72, v106
	v_add_f32_e32 v69, v69, v109
	v_cvt_pk_f16_f32 v82, v66, v67
	v_add_f32_e32 v66, v73, v107
	v_cvt_pk_f16_f32 v68, v68, v69
	v_cvt_pk_f16_f32 v69, v70, v71
	v_cvt_pk_f16_f32 v70, v72, v66
	v_cndmask_b32_e64 v66, v68, v70, s[0:1]
	v_cndmask_b32_e64 v67, v82, v69, s[0:1]
	ds_bpermute_b32 v71, v144, v66
	ds_bpermute_b32 v72, v144, v67
	v_lshl_add_u32 v118, v143, 7, v133
	v_add_u32_e32 v130, s4, v118
	v_lshlrev_b64 v[66:67], 5, v[130:131]
	v_lshl_add_u64 v[66:67], v[0:1], 0, v[66:67]
	global_store_dwordx4 v[66:67], v[98:101], off
	s_waitcnt lgkmcnt(1)
	v_cndmask_b32_e64 v67, v71, v68, s[0:1]
	v_cndmask_b32_e64 v68, v70, v71, s[0:1]
	s_waitcnt lgkmcnt(0)
	v_cndmask_b32_e64 v70, v69, v72, s[0:1]
	v_cndmask_b32_e64 v71, v120, v70, s[0:1]
	v_cndmask_b32_e64 v69, v121, v68, s[0:1]
	v_cndmask_b32_e64 v66, v72, v82, s[0:1]
	v_bfi_b32 v69, s2, v68, v69
	v_bfi_b32 v68, s2, v71, v70
	ds_read2st64_b32 v[70:71], v110 offset0:8 offset1:9
	ds_read2st64_b32 v[72:73], v110 offset0:12 offset1:13
	ds_read2st64_b32 v[82:83], v110 offset0:14 offset1:15
	ds_read2st64_b32 v[84:85], v110 offset0:10 offset1:11
	s_waitcnt lgkmcnt(3)
	v_add_f32_e32 v70, v74, v70
	v_add_f32_e32 v71, v75, v71
	s_waitcnt lgkmcnt(2)
	v_add_f32_e32 v73, v79, v73
	v_add_f32_e32 v72, v78, v72
	s_waitcnt lgkmcnt(0)
	v_add_f32_e32 v74, v76, v84
	v_add_f32_e32 v75, v80, v82
	v_add_f32_e32 v76, v77, v85
	v_cvt_pk_f16_f32 v78, v70, v71
	v_add_f32_e32 v70, v81, v83
	v_cvt_pk_f16_f32 v74, v74, v76
	v_cvt_pk_f16_f32 v72, v72, v73
	v_cvt_pk_f16_f32 v73, v75, v70
	v_cndmask_b32_e64 v70, v74, v73, s[0:1]
	v_cndmask_b32_e64 v71, v78, v72, s[0:1]
	ds_bpermute_b32 v75, v144, v70
	ds_bpermute_b32 v76, v144, v71
	v_add_u32_e32 v130, s5, v119
	v_lshlrev_b64 v[70:71], 5, v[130:131]
	v_lshl_add_u64 v[70:71], v[0:1], 0, v[70:71]
	global_store_dwordx4 v[70:71], v[66:69], off
	s_waitcnt lgkmcnt(0)
	v_cndmask_b32_e64 v70, v72, v76, s[0:1]
	v_cndmask_b32_e64 v71, v120, v70, s[0:1]
	v_cndmask_b32_e64 v68, v73, v75, s[0:1]
	v_cndmask_b32_e64 v69, v121, v68, s[0:1]
	v_add_u32_e32 v130, s6, v118
	v_bfi_b32 v69, s2, v68, v69
	v_bfi_b32 v68, s2, v71, v70
	v_lshlrev_b64 v[70:71], 5, v[130:131]
	v_cndmask_b32_e64 v67, v75, v74, s[0:1]
	v_cndmask_b32_e64 v66, v76, v78, s[0:1]
	v_lshl_add_u64 v[70:71], v[0:1], 0, v[70:71]
	v_xor_b32_e32 v50, 0x6000, v141
	global_store_dwordx4 v[70:71], v[66:69], off
	v_or_b32_e32 v74, v140, v50
	ds_read2st64_b32 v[66:67], v74 offset1:1
	ds_read2st64_b32 v[68:69], v74 offset0:4 offset1:5
	ds_read2st64_b32 v[70:71], v74 offset0:6 offset1:7
	ds_read2st64_b32 v[72:73], v74 offset0:2 offset1:3
	s_waitcnt lgkmcnt(3)
	v_add_f32_e32 v34, v34, v66
	v_add_f32_e32 v35, v35, v67
	s_waitcnt lgkmcnt(0)
	v_add_f32_e32 v36, v36, v72
	v_add_f32_e32 v37, v37, v73
	v_add_f32_e32 v38, v38, v68
	v_add_f32_e32 v39, v39, v69
	v_add_f32_e32 v40, v40, v70
	v_cvt_pk_f16_f32 v34, v34, v35
	v_cvt_pk_f16_f32 v35, v36, v37
	v_add_f32_e32 v36, v41, v71
	v_cvt_pk_f16_f32 v37, v38, v39
	v_cvt_pk_f16_f32 v36, v40, v36
	v_cndmask_b32_e64 v38, v35, v36, s[0:1]
	v_cndmask_b32_e64 v39, v34, v37, s[0:1]
	ds_bpermute_b32 v38, v144, v38
	ds_bpermute_b32 v39, v144, v39
	v_or_b32_e32 v40, 1, v143
	v_lshl_add_u32 v54, v40, 7, v133
	v_or_b32_e32 v55, v40, v145
	s_waitcnt lgkmcnt(1)
	v_cndmask_b32_e64 v35, v38, v35, s[0:1]
	v_cndmask_b32_e64 v36, v36, v38, s[0:1]
	s_waitcnt lgkmcnt(0)
	v_cndmask_b32_e64 v38, v37, v39, s[0:1]
	v_cndmask_b32_e64 v34, v39, v34, s[0:1]
	v_cndmask_b32_e64 v39, v120, v38, s[0:1]
	v_cndmask_b32_e64 v37, v121, v36, s[0:1]
	v_bfi_b32 v37, s2, v36, v37
	v_bfi_b32 v36, s2, v39, v38
	ds_read2st64_b32 v[38:39], v74 offset0:8 offset1:9
	ds_read2st64_b32 v[40:41], v74 offset0:12 offset1:13
	ds_read2st64_b32 v[50:51], v74 offset0:14 offset1:15
	ds_read2st64_b32 v[52:53], v74 offset0:10 offset1:11
	s_waitcnt lgkmcnt(3)
	v_add_f32_e32 v38, v42, v38
	v_add_f32_e32 v39, v43, v39
	s_waitcnt lgkmcnt(2)
	v_add_f32_e32 v41, v47, v41
	v_add_f32_e32 v40, v46, v40
	s_waitcnt lgkmcnt(0)
	v_add_f32_e32 v42, v44, v52
	v_add_f32_e32 v43, v48, v50
	v_add_f32_e32 v44, v45, v53
	v_cvt_pk_f16_f32 v46, v38, v39
	v_add_f32_e32 v38, v49, v51
	v_cvt_pk_f16_f32 v42, v42, v44
	v_cvt_pk_f16_f32 v40, v40, v41
	v_cvt_pk_f16_f32 v41, v43, v38
	v_cndmask_b32_e64 v38, v42, v41, s[0:1]
	v_cndmask_b32_e64 v39, v46, v40, s[0:1]
	ds_bpermute_b32 v43, v144, v38
	ds_bpermute_b32 v44, v144, v39
	v_add_u32_e32 v130, s3, v55
	v_lshlrev_b64 v[38:39], 5, v[130:131]
	v_lshl_add_u64 v[38:39], v[0:1], 0, v[38:39]
	global_store_dwordx4 v[38:39], v[34:37], off
	s_waitcnt lgkmcnt(0)
	v_cndmask_b32_e64 v38, v40, v44, s[0:1]
	v_cndmask_b32_e64 v36, v41, v43, s[0:1]
	v_xor_b32_e32 v18, 0x7000, v141
	v_cndmask_b32_e64 v39, v120, v38, s[0:1]
	v_cndmask_b32_e64 v37, v121, v36, s[0:1]
	v_or_b32_e32 v18, v140, v18
	v_cndmask_b32_e64 v35, v43, v42, s[0:1]
	v_cndmask_b32_e64 v34, v44, v46, s[0:1]
	v_bfi_b32 v37, s2, v36, v37
	v_bfi_b32 v36, s2, v39, v38
	ds_read2st64_b32 v[38:39], v18 offset1:1
	ds_read2st64_b32 v[40:41], v18 offset0:4 offset1:5
	ds_read2st64_b32 v[42:43], v18 offset0:6 offset1:7
	ds_read2st64_b32 v[44:45], v18 offset0:2 offset1:3
	s_waitcnt lgkmcnt(3)
	v_add_f32_e32 v2, v2, v38
	v_add_f32_e32 v3, v3, v39
	s_waitcnt lgkmcnt(2)
	v_add_f32_e32 v6, v6, v40
	v_add_f32_e32 v7, v7, v41
	s_waitcnt lgkmcnt(0)
	v_add_f32_e32 v4, v4, v44
	v_add_f32_e32 v8, v8, v42
	v_add_f32_e32 v5, v5, v45
	v_cvt_pk_f16_f32 v19, v2, v3
	v_add_f32_e32 v2, v9, v43
	v_cvt_pk_f16_f32 v4, v4, v5
	v_cvt_pk_f16_f32 v5, v6, v7
	v_cvt_pk_f16_f32 v6, v8, v2
	v_cndmask_b32_e64 v2, v4, v6, s[0:1]
	v_cndmask_b32_e64 v3, v19, v5, s[0:1]
	ds_bpermute_b32 v7, v144, v2
	ds_bpermute_b32 v8, v144, v3
	v_add_u32_e32 v130, s4, v54
	v_lshlrev_b64 v[2:3], 5, v[130:131]
	v_lshl_add_u64 v[2:3], v[0:1], 0, v[2:3]
	global_store_dwordx4 v[2:3], v[34:37], off
	s_waitcnt lgkmcnt(1)
	v_cndmask_b32_e64 v3, v7, v4, s[0:1]
	v_cndmask_b32_e64 v4, v6, v7, s[0:1]
	s_waitcnt lgkmcnt(0)
	v_cndmask_b32_e64 v6, v5, v8, s[0:1]
	v_cndmask_b32_e64 v7, v120, v6, s[0:1]
	v_cndmask_b32_e64 v5, v121, v4, s[0:1]
	v_cndmask_b32_e64 v2, v8, v19, s[0:1]
	v_bfi_b32 v5, s2, v4, v5
	v_bfi_b32 v4, s2, v7, v6
	ds_read2st64_b32 v[6:7], v18 offset0:8 offset1:9
	ds_read2st64_b32 v[8:9], v18 offset0:12 offset1:13
	v_mov_b32_e32 v19, v10
	v_mov_b32_e32 v21, v11
	ds_read2st64_b32 v[10:11], v18 offset0:14 offset1:15
	v_mov_b32_e32 v20, v14
	v_mov_b32_e32 v22, v15
	ds_read2st64_b32 v[14:15], v18 offset0:10 offset1:11
	s_waitcnt lgkmcnt(3)
	v_add_f32_e32 v6, v19, v6
	v_add_f32_e32 v7, v21, v7
	s_waitcnt lgkmcnt(2)
	v_add_f32_e32 v8, v20, v8
	v_add_f32_e32 v9, v22, v9
	s_waitcnt lgkmcnt(1)
	v_add_f32_e32 v10, v16, v10
	s_waitcnt lgkmcnt(0)
	v_add_f32_e32 v12, v12, v14
	v_add_f32_e32 v13, v13, v15
	v_cvt_pk_f16_f32 v14, v6, v7
	v_add_f32_e32 v6, v17, v11
	v_cvt_pk_f16_f32 v12, v12, v13
	v_cvt_pk_f16_f32 v8, v8, v9
	v_cvt_pk_f16_f32 v9, v10, v6
	v_cndmask_b32_e64 v6, v12, v9, s[0:1]
	v_cndmask_b32_e64 v7, v14, v8, s[0:1]
	ds_bpermute_b32 v10, v144, v6
	ds_bpermute_b32 v11, v144, v7
	v_add_u32_e32 v130, s5, v55
	v_lshlrev_b64 v[6:7], 5, v[130:131]
	v_lshl_add_u64 v[6:7], v[0:1], 0, v[6:7]
	global_store_dwordx4 v[6:7], v[2:5], off
	s_waitcnt lgkmcnt(0)
	v_cndmask_b32_e64 v6, v8, v11, s[0:1]
	v_cndmask_b32_e64 v7, v120, v6, s[0:1]
	v_cndmask_b32_e64 v4, v9, v10, s[0:1]
	v_cndmask_b32_e64 v5, v121, v4, s[0:1]
	v_add_u32_e32 v130, s6, v54
	v_bfi_b32 v5, s2, v4, v5
	v_bfi_b32 v4, s2, v7, v6
	v_lshlrev_b64 v[6:7], 5, v[130:131]
	v_cndmask_b32_e64 v3, v10, v12, s[0:1]
	v_cndmask_b32_e64 v2, v11, v14, s[0:1]
	v_lshl_add_u64 v[0:1], v[0:1], 0, v[6:7]
	global_store_dwordx4 v[0:1], v[2:5], off
	s_endpgm
.Lk1_role1:
	ds_write2st64_b32 v130, v98, v99 offset1:1
	ds_write2st64_b32 v130, v100, v101 offset0:2 offset1:3
	ds_write2st64_b32 v130, v102, v103 offset0:4 offset1:5
	ds_write2st64_b32 v130, v104, v105 offset0:6 offset1:7
	ds_write2st64_b32 v130, v106, v107 offset0:8 offset1:9
	ds_write2st64_b32 v130, v108, v109 offset0:10 offset1:11
	v_cvt_pk_f16_f32 v147, v171, v179
	v_cvt_pk_f16_f32 v146, v187, v167
	v_cvt_pk_f16_f32 v145, v191, v183
	v_cvt_pk_f16_f32 v144, v155, v195
	ds_write2st64_b32 v130, v110, v111 offset0:12 offset1:13
	s_nop 1
	v_mfma_f32_32x32x16_f16 v[50:65], v[148:151], v[144:147], v[50:65]
	ds_write2st64_b32 v130, v112, v113 offset0:14 offset1:15
	ds_write2st64_b32 v130, v66, v67 offset0:16 offset1:17
	ds_write2st64_b32 v130, v68, v69 offset0:18 offset1:19
	ds_write2st64_b32 v130, v70, v71 offset0:20 offset1:21
	ds_write2st64_b32 v130, v72, v73 offset0:22 offset1:23
	ds_write2st64_b32 v130, v74, v75 offset0:24 offset1:25
	ds_write2st64_b32 v130, v76, v77 offset0:26 offset1:27
	ds_write2st64_b32 v130, v78, v79 offset0:28 offset1:29
	s_nop 1
	v_mfma_f32_32x32x16_f16 v[18:33], v[136:139], v[144:147], v[18:33]
	s_nop 11
	ds_write2st64_b32 v130, v80, v81 offset0:30 offset1:31
	ds_write2st64_b32 v130, v34, v35 offset0:32 offset1:33
	ds_write2st64_b32 v130, v36, v37 offset0:34 offset1:35
	ds_write2st64_b32 v130, v38, v39 offset0:36 offset1:37
	ds_write2st64_b32 v130, v40, v41 offset0:38 offset1:39
	ds_write2st64_b32 v130, v42, v43 offset0:40 offset1:41
	ds_write2st64_b32 v130, v44, v45 offset0:42 offset1:43
	ds_write2st64_b32 v130, v46, v47 offset0:44 offset1:45
	ds_write2st64_b32 v130, v48, v49 offset0:46 offset1:47
	ds_write2st64_b32 v130, v2, v3 offset0:48 offset1:49
	ds_write2st64_b32 v130, v4, v5 offset0:50 offset1:51
	ds_write2st64_b32 v130, v6, v7 offset0:52 offset1:53
	ds_write2st64_b32 v130, v8, v9 offset0:54 offset1:55
	ds_write2st64_b32 v130, v10, v11 offset0:56 offset1:57
	ds_write2st64_b32 v130, v12, v13 offset0:58 offset1:59
	ds_write2st64_b32 v130, v14, v15 offset0:60 offset1:61
	ds_write2st64_b32 v130, v16, v17 offset0:62 offset1:63
	v_lshlrev_b32_e32 v0, 2, v1
	v_lshl_or_b32 v143, v135, 1, v0
	v_mbcnt_lo_u32_b32 v0, -1, 0
	v_mbcnt_hi_u32_b32 v0, -1, v0
	v_and_b32_e32 v130, 64, v0
	v_xor_b32_e32 v1, 32, v0
	v_add_u32_e32 v130, 64, v130
	v_cmp_lt_i32_e64 s[0:1], v1, v130
	v_lshlrev_b32_e32 v130, 1, v142
	s_waitcnt lgkmcnt(0)
	v_cndmask_b32_e64 v0, v0, v1, s[0:1]
	v_lshlrev_b32_e32 v144, 2, v0
	v_xor_b32_e32 v0, 0x4000, v141
	v_or_b32_e32 v142, v140, v0
	s_barrier
	ds_read2st64_b32 v[0:1], v142 offset1:1
	ds_read2st64_b32 v[134:135], v142 offset0:4 offset1:5
	ds_read2st64_b32 v[136:137], v142 offset0:6 offset1:7
	ds_read2st64_b32 v[138:139], v142 offset0:2 offset1:3
	s_waitcnt lgkmcnt(3)
	v_add_f32_e32 v0, v114, v0
	s_waitcnt lgkmcnt(2)
	v_add_f32_e32 v98, v118, v134
	v_add_f32_e32 v1, v115, v1
	v_add_f32_e32 v99, v119, v135
	s_waitcnt lgkmcnt(0)
	v_add_f32_e32 v100, v116, v138
	v_add_f32_e32 v102, v120, v136
	v_add_f32_e32 v101, v117, v139
	v_cvt_pk_f16_f32 v104, v0, v1
	v_add_f32_e32 v0, v121, v137
	v_cvt_pk_f16_f32 v100, v100, v101
	v_cvt_pk_f16_f32 v101, v98, v99
	v_cvt_pk_f16_f32 v102, v102, v0
	v_cmp_gt_u32_e64 s[0:1], 32, v132
	v_mov_b32_e32 v120, 0x3c00
	v_mov_b32_e32 v103, v121
	v_bfrev_b32_e32 v121, 60
	v_cndmask_b32_e64 v0, v100, v102, s[0:1]
	v_cndmask_b32_e64 v1, v104, v101, s[0:1]
	ds_bpermute_b32 v103, v144, v0
	ds_bpermute_b32 v105, v144, v1
	v_lshlrev_b32_e32 v145, 7, v133
	s_waitcnt lgkmcnt(1)
	v_cndmask_b32_e64 v99, v103, v100, s[0:1]
	v_cndmask_b32_e64 v100, v102, v103, s[0:1]
	s_waitcnt lgkmcnt(0)
	v_cndmask_b32_e64 v102, v101, v105, s[0:1]
	v_cndmask_b32_e64 v103, v120, v102, s[0:1]
	v_cndmask_b32_e64 v101, v121, v100, s[0:1]
	v_cndmask_b32_e64 v98, v105, v104, s[0:1]
	v_bfi_b32 v101, s2, v100, v101
	v_bfi_b32 v100, s2, v103, v102
	ds_read2st64_b32 v[102:103], v142 offset0:8 offset1:9
	ds_read2st64_b32 v[104:105], v142 offset0:12 offset1:13
	ds_read2st64_b32 v[114:115], v142 offset0:14 offset1:15
	ds_read2st64_b32 v[116:117], v142 offset0:10 offset1:11
	v_or_b32_e32 v119, v143, v145
	v_lshl_add_u64 v[0:1], s[8:9], 0, v[130:131]
	s_waitcnt lgkmcnt(3)
	v_add_f32_e32 v102, v122, v102
	v_add_f32_e32 v103, v123, v103
	s_waitcnt lgkmcnt(2)
	v_add_f32_e32 v105, v127, v105
	v_add_f32_e32 v104, v126, v104
	s_waitcnt lgkmcnt(0)
	v_add_f32_e32 v106, v124, v116
	v_add_f32_e32 v107, v128, v114
	v_add_f32_e32 v108, v125, v117
	v_cvt_pk_f16_f32 v110, v102, v103
	v_add_f32_e32 v102, v129, v115
	v_cvt_pk_f16_f32 v106, v106, v108
	v_cvt_pk_f16_f32 v104, v104, v105
	v_cvt_pk_f16_f32 v105, v107, v102
	v_cndmask_b32_e64 v102, v106, v105, s[0:1]
	v_cndmask_b32_e64 v103, v110, v104, s[0:1]
	ds_bpermute_b32 v107, v144, v102
	ds_bpermute_b32 v108, v144, v103
	v_add_u32_e32 v130, s3, v119
	v_lshlrev_b64 v[102:103], 5, v[130:131]
	v_lshl_add_u64 v[102:103], v[0:1], 0, v[102:103]
	global_store_dwordx4 v[102:103], v[98:101], off
	s_waitcnt lgkmcnt(0)
	v_cndmask_b32_e64 v102, v104, v108, s[0:1]
	v_cndmask_b32_e64 v100, v105, v107, s[0:1]
	v_mov_b32_e32 v66, v82
	v_xor_b32_e32 v82, 0x5000, v141
	v_cndmask_b32_e64 v98, v108, v110, s[0:1]
	v_cndmask_b32_e64 v103, v120, v102, s[0:1]
	v_cndmask_b32_e64 v101, v121, v100, s[0:1]
	v_or_b32_e32 v110, v140, v82
	v_cndmask_b32_e64 v99, v107, v106, s[0:1]
	v_bfi_b32 v101, s2, v100, v101
	v_bfi_b32 v100, s2, v103, v102
	ds_read2st64_b32 v[102:103], v110 offset1:1
	ds_read2st64_b32 v[104:105], v110 offset0:4 offset1:5
	ds_read2st64_b32 v[106:107], v110 offset0:6 offset1:7
	ds_read2st64_b32 v[108:109], v110 offset0:2 offset1:3
	s_waitcnt lgkmcnt(3)
	v_add_f32_e32 v66, v66, v102
	v_add_f32_e32 v67, v83, v103
	s_waitcnt lgkmcnt(2)
	v_add_f32_e32 v70, v86, v104
	v_add_f32_e32 v71, v87, v105
	s_waitcnt lgkmcnt(0)
	v_add_f32_e32 v68, v84, v108
	v_add_f32_e32 v72, v88, v106
	v_add_f32_e32 v69, v85, v109
	v_cvt_pk_f16_f32 v82, v66, v67
	v_add_f32_e32 v66, v89, v107
	v_cvt_pk_f16_f32 v68, v68, v69
	v_cvt_pk_f16_f32 v69, v70, v71
	v_cvt_pk_f16_f32 v70, v72, v66
	v_cndmask_b32_e64 v66, v68, v70, s[0:1]
	v_cndmask_b32_e64 v67, v82, v69, s[0:1]
	ds_bpermute_b32 v71, v144, v66
	ds_bpermute_b32 v72, v144, v67
	v_lshl_add_u32 v118, v143, 7, v133
	v_add_u32_e32 v130, s4, v118
	v_lshlrev_b64 v[66:67], 5, v[130:131]
	v_lshl_add_u64 v[66:67], v[0:1], 0, v[66:67]
	global_store_dwordx4 v[66:67], v[98:101], off
	s_waitcnt lgkmcnt(1)
	v_cndmask_b32_e64 v67, v71, v68, s[0:1]
	v_cndmask_b32_e64 v68, v70, v71, s[0:1]
	s_waitcnt lgkmcnt(0)
	v_cndmask_b32_e64 v70, v69, v72, s[0:1]
	v_cndmask_b32_e64 v71, v120, v70, s[0:1]
	v_cndmask_b32_e64 v69, v121, v68, s[0:1]
	v_cndmask_b32_e64 v66, v72, v82, s[0:1]
	v_bfi_b32 v69, s2, v68, v69
	v_bfi_b32 v68, s2, v71, v70
	ds_read2st64_b32 v[70:71], v110 offset0:8 offset1:9
	ds_read2st64_b32 v[72:73], v110 offset0:12 offset1:13
	ds_read2st64_b32 v[82:83], v110 offset0:14 offset1:15
	ds_read2st64_b32 v[84:85], v110 offset0:10 offset1:11
	s_waitcnt lgkmcnt(3)
	v_add_f32_e32 v70, v90, v70
	v_add_f32_e32 v71, v91, v71
	s_waitcnt lgkmcnt(2)
	v_add_f32_e32 v73, v95, v73
	v_add_f32_e32 v72, v94, v72
	s_waitcnt lgkmcnt(0)
	v_add_f32_e32 v74, v92, v84
	v_add_f32_e32 v75, v96, v82
	v_add_f32_e32 v76, v93, v85
	v_cvt_pk_f16_f32 v78, v70, v71
	v_add_f32_e32 v70, v97, v83
	v_cvt_pk_f16_f32 v74, v74, v76
	v_cvt_pk_f16_f32 v72, v72, v73
	v_cvt_pk_f16_f32 v73, v75, v70
	v_cndmask_b32_e64 v70, v74, v73, s[0:1]
	v_cndmask_b32_e64 v71, v78, v72, s[0:1]
	ds_bpermute_b32 v75, v144, v70
	ds_bpermute_b32 v76, v144, v71
	v_add_u32_e32 v130, s5, v119
	v_lshlrev_b64 v[70:71], 5, v[130:131]
	v_lshl_add_u64 v[70:71], v[0:1], 0, v[70:71]
	global_store_dwordx4 v[70:71], v[66:69], off
	s_waitcnt lgkmcnt(0)
	v_cndmask_b32_e64 v70, v72, v76, s[0:1]
	v_cndmask_b32_e64 v71, v120, v70, s[0:1]
	v_cndmask_b32_e64 v68, v73, v75, s[0:1]
	v_cndmask_b32_e64 v69, v121, v68, s[0:1]
	v_add_u32_e32 v130, s6, v118
	v_bfi_b32 v69, s2, v68, v69
	v_bfi_b32 v68, s2, v71, v70
	v_lshlrev_b64 v[70:71], 5, v[130:131]
	v_cndmask_b32_e64 v67, v75, v74, s[0:1]
	v_cndmask_b32_e64 v66, v76, v78, s[0:1]
	v_lshl_add_u64 v[70:71], v[0:1], 0, v[70:71]
	v_mov_b32_e32 v34, v50
	v_xor_b32_e32 v50, 0x6000, v141
	global_store_dwordx4 v[70:71], v[66:69], off
	v_or_b32_e32 v74, v140, v50
	ds_read2st64_b32 v[66:67], v74 offset1:1
	ds_read2st64_b32 v[68:69], v74 offset0:4 offset1:5
	ds_read2st64_b32 v[70:71], v74 offset0:6 offset1:7
	ds_read2st64_b32 v[72:73], v74 offset0:2 offset1:3
	s_waitcnt lgkmcnt(3)
	v_add_f32_e32 v34, v34, v66
	v_add_f32_e32 v35, v51, v67
	s_waitcnt lgkmcnt(0)
	v_add_f32_e32 v36, v52, v72
	v_add_f32_e32 v37, v53, v73
	v_add_f32_e32 v38, v54, v68
	v_add_f32_e32 v39, v55, v69
	v_add_f32_e32 v40, v56, v70
	v_cvt_pk_f16_f32 v34, v34, v35
	v_cvt_pk_f16_f32 v35, v36, v37
	v_add_f32_e32 v36, v57, v71
	v_cvt_pk_f16_f32 v37, v38, v39
	v_cvt_pk_f16_f32 v36, v40, v36
	v_cndmask_b32_e64 v38, v35, v36, s[0:1]
	v_cndmask_b32_e64 v39, v34, v37, s[0:1]
	ds_bpermute_b32 v38, v144, v38
	ds_bpermute_b32 v39, v144, v39
	v_or_b32_e32 v40, 1, v143
	v_lshl_add_u32 v54, v40, 7, v133
	v_or_b32_e32 v55, v40, v145
	s_waitcnt lgkmcnt(1)
	v_cndmask_b32_e64 v35, v38, v35, s[0:1]
	v_cndmask_b32_e64 v36, v36, v38, s[0:1]
	s_waitcnt lgkmcnt(0)
	v_cndmask_b32_e64 v38, v37, v39, s[0:1]
	v_cndmask_b32_e64 v34, v39, v34, s[0:1]
	v_cndmask_b32_e64 v39, v120, v38, s[0:1]
	v_cndmask_b32_e64 v37, v121, v36, s[0:1]
	v_bfi_b32 v37, s2, v36, v37
	v_bfi_b32 v36, s2, v39, v38
	ds_read2st64_b32 v[38:39], v74 offset0:8 offset1:9
	ds_read2st64_b32 v[40:41], v74 offset0:12 offset1:13
	ds_read2st64_b32 v[50:51], v74 offset0:14 offset1:15
	ds_read2st64_b32 v[52:53], v74 offset0:10 offset1:11
	s_waitcnt lgkmcnt(3)
	v_add_f32_e32 v38, v58, v38
	v_add_f32_e32 v39, v59, v39
	s_waitcnt lgkmcnt(2)
	v_add_f32_e32 v41, v63, v41
	v_add_f32_e32 v40, v62, v40
	s_waitcnt lgkmcnt(0)
	v_add_f32_e32 v42, v60, v52
	v_add_f32_e32 v43, v64, v50
	v_add_f32_e32 v44, v61, v53
	v_cvt_pk_f16_f32 v46, v38, v39
	v_add_f32_e32 v38, v65, v51
	v_cvt_pk_f16_f32 v42, v42, v44
	v_cvt_pk_f16_f32 v40, v40, v41
	v_cvt_pk_f16_f32 v41, v43, v38
	v_cndmask_b32_e64 v38, v42, v41, s[0:1]
	v_cndmask_b32_e64 v39, v46, v40, s[0:1]
	ds_bpermute_b32 v43, v144, v38
	ds_bpermute_b32 v44, v144, v39
	v_add_u32_e32 v130, s3, v55
	v_lshlrev_b64 v[38:39], 5, v[130:131]
	v_lshl_add_u64 v[38:39], v[0:1], 0, v[38:39]
	global_store_dwordx4 v[38:39], v[34:37], off
	s_waitcnt lgkmcnt(0)
	v_cndmask_b32_e64 v38, v40, v44, s[0:1]
	v_cndmask_b32_e64 v36, v41, v43, s[0:1]
	v_mov_b32_e32 v2, v18
	v_xor_b32_e32 v18, 0x7000, v141
	v_cndmask_b32_e64 v39, v120, v38, s[0:1]
	v_cndmask_b32_e64 v37, v121, v36, s[0:1]
	v_or_b32_e32 v18, v140, v18
	v_cndmask_b32_e64 v35, v43, v42, s[0:1]
	v_cndmask_b32_e64 v34, v44, v46, s[0:1]
	v_bfi_b32 v37, s2, v36, v37
	v_bfi_b32 v36, s2, v39, v38
	ds_read2st64_b32 v[38:39], v18 offset1:1
	ds_read2st64_b32 v[40:41], v18 offset0:4 offset1:5
	ds_read2st64_b32 v[42:43], v18 offset0:6 offset1:7
	ds_read2st64_b32 v[44:45], v18 offset0:2 offset1:3
	s_waitcnt lgkmcnt(3)
	v_add_f32_e32 v2, v2, v38
	v_add_f32_e32 v3, v19, v39
	s_waitcnt lgkmcnt(2)
	v_add_f32_e32 v6, v22, v40
	v_add_f32_e32 v7, v23, v41
	s_waitcnt lgkmcnt(0)
	v_add_f32_e32 v4, v20, v44
	v_add_f32_e32 v8, v24, v42
	v_add_f32_e32 v5, v21, v45
	v_cvt_pk_f16_f32 v19, v2, v3
	v_add_f32_e32 v2, v25, v43
	v_cvt_pk_f16_f32 v4, v4, v5
	v_cvt_pk_f16_f32 v5, v6, v7
	v_cvt_pk_f16_f32 v6, v8, v2
	v_cndmask_b32_e64 v2, v4, v6, s[0:1]
	v_cndmask_b32_e64 v3, v19, v5, s[0:1]
	ds_bpermute_b32 v7, v144, v2
	ds_bpermute_b32 v8, v144, v3
	v_add_u32_e32 v130, s4, v54
	v_lshlrev_b64 v[2:3], 5, v[130:131]
	v_lshl_add_u64 v[2:3], v[0:1], 0, v[2:3]
	global_store_dwordx4 v[2:3], v[34:37], off
	s_waitcnt lgkmcnt(1)
	v_cndmask_b32_e64 v3, v7, v4, s[0:1]
	v_cndmask_b32_e64 v4, v6, v7, s[0:1]
	s_waitcnt lgkmcnt(0)
	v_cndmask_b32_e64 v6, v5, v8, s[0:1]
	v_cndmask_b32_e64 v7, v120, v6, s[0:1]
	v_cndmask_b32_e64 v5, v121, v4, s[0:1]
	v_cndmask_b32_e64 v2, v8, v19, s[0:1]
	v_bfi_b32 v5, s2, v4, v5
	v_bfi_b32 v4, s2, v7, v6
	ds_read2st64_b32 v[6:7], v18 offset0:8 offset1:9
	ds_read2st64_b32 v[8:9], v18 offset0:12 offset1:13
	ds_read2st64_b32 v[10:11], v18 offset0:14 offset1:15
	ds_read2st64_b32 v[14:15], v18 offset0:10 offset1:11
	s_waitcnt lgkmcnt(3)
	v_add_f32_e32 v6, v26, v6
	v_add_f32_e32 v7, v27, v7
	s_waitcnt lgkmcnt(2)
	v_add_f32_e32 v8, v30, v8
	v_add_f32_e32 v9, v31, v9
	s_waitcnt lgkmcnt(1)
	v_add_f32_e32 v10, v32, v10
	s_waitcnt lgkmcnt(0)
	v_add_f32_e32 v12, v28, v14
	v_add_f32_e32 v13, v29, v15
	v_cvt_pk_f16_f32 v14, v6, v7
	v_add_f32_e32 v6, v33, v11
	v_cvt_pk_f16_f32 v12, v12, v13
	v_cvt_pk_f16_f32 v8, v8, v9
	v_cvt_pk_f16_f32 v9, v10, v6
	v_cndmask_b32_e64 v6, v12, v9, s[0:1]
	v_cndmask_b32_e64 v7, v14, v8, s[0:1]
	ds_bpermute_b32 v10, v144, v6
	ds_bpermute_b32 v11, v144, v7
	v_add_u32_e32 v130, s5, v55
	v_lshlrev_b64 v[6:7], 5, v[130:131]
	v_lshl_add_u64 v[6:7], v[0:1], 0, v[6:7]
	global_store_dwordx4 v[6:7], v[2:5], off
	s_waitcnt lgkmcnt(0)
	v_cndmask_b32_e64 v6, v8, v11, s[0:1]
	v_cndmask_b32_e64 v7, v120, v6, s[0:1]
	v_cndmask_b32_e64 v4, v9, v10, s[0:1]
	v_cndmask_b32_e64 v5, v121, v4, s[0:1]
	v_add_u32_e32 v130, s6, v54
	v_bfi_b32 v5, s2, v4, v5
	v_bfi_b32 v4, s2, v7, v6
	v_lshlrev_b64 v[6:7], 5, v[130:131]
	v_cndmask_b32_e64 v3, v10, v12, s[0:1]
	v_cndmask_b32_e64 v2, v11, v14, s[0:1]
	v_lshl_add_u64 v[0:1], v[0:1], 0, v[6:7]
	global_store_dwordx4 v[0:1], v[2:5], off
	s_endpgm
